# final grid barrier after the last phase removed (kernel ends there), code warm-up loads limited to barriers 1-36
# baseline (speedup 1.0000x reference)
.LBB0_3663:
	s_waitcnt lgkmcnt(0)
	s_barrier
	s_waitcnt vmcnt(0)
	s_barrier
	s_mov_b64 s[0:1], exec
	v_readlane_b32 s2, v242, 7
	v_readlane_b32 s3, v242, 8
	s_and_b64 s[2:3], s[0:1], s[2:3]
	s_mov_b64 exec, s[2:3]
	s_cbranch_execz .LBB0_3715
	s_add_i32 s2, 0, 0x20000
	s_waitcnt vmcnt(6)
	v_mov_b32_e32 v0, s2
	s_waitcnt vmcnt(0) expcnt(0) lgkmcnt(0)
	ds_read_b32 v2, v0
	s_add_i32 s2, 0, 0x20004
	v_mov_b32_e32 v0, s2
	ds_read_b32 v0, v0
	s_waitcnt lgkmcnt(1)
	v_cmp_ne_u32_e32 vcc, 0, v2
	s_cbranch_vccnz .LBB0_3679
	v_readlane_b32 s2, v242, 9
	v_readlane_b32 s3, v242, 10
	s_load_dwordx2 s[6:7], s[2:3], 0x4
	s_add_u32 s2, s96, 0x1000
	s_addc_u32 s3, s97, 0
	s_add_u32 s4, s96, 0x1100
	s_addc_u32 s5, s97, 0
	v_readlane_b32 s8, v242, 11
	s_waitcnt lgkmcnt(0)
	s_mul_i32 s16, s6, s8
	s_add_u32 s6, s96, 0x1200
	s_mul_i32 s16, s16, s7
	s_addc_u32 s7, s97, 0
	v_readlane_b32 s9, v242, 12
	s_add_u32 s8, s96, 0x1300
	s_addc_u32 s9, s97, 0
	s_mov_b32 s17, 1
	v_mov_b32_e32 v16, 0
	s_branch .LBB0_3667

.LBB0_3847:
	s_barrier
	s_waitcnt vmcnt(0)
	s_barrier
	s_mov_b64 s[0:1], exec
	v_readlane_b32 s2, v242, 7
	v_readlane_b32 s3, v242, 8
	s_and_b64 s[2:3], s[0:1], s[2:3]
	s_mov_b64 exec, s[2:3]
	s_cbranch_execz .LBB0_3899
	s_add_i32 s2, 0, 0x20000
	v_mov_b32_e32 v0, s2
	s_waitcnt vmcnt(0) expcnt(0) lgkmcnt(0)
	ds_read_b32 v2, v0
	s_add_i32 s2, 0, 0x20004
	v_mov_b32_e32 v0, s2
	ds_read_b32 v0, v0
	s_waitcnt lgkmcnt(1)
	v_cmp_ne_u32_e32 vcc, 0, v2
	s_cbranch_vccnz .LBB0_3863
	v_readlane_b32 s2, v242, 9
	v_readlane_b32 s3, v242, 10
	s_load_dwordx2 s[6:7], s[2:3], 0x4
	s_add_u32 s2, s96, 0x1000
	s_addc_u32 s3, s97, 0
	s_add_u32 s4, s96, 0x1100
	s_addc_u32 s5, s97, 0
	v_readlane_b32 s8, v242, 11
	s_waitcnt lgkmcnt(0)
	s_mul_i32 s16, s6, s8
	s_add_u32 s6, s96, 0x1200
	s_mul_i32 s16, s16, s7
	s_addc_u32 s7, s97, 0
	v_readlane_b32 s9, v242, 12
	s_add_u32 s8, s96, 0x1300
	s_addc_u32 s9, s97, 0
	s_mov_b32 s17, 1
	v_mov_b32_e32 v16, 0
	s_branch .LBB0_3851

.LBB0_4061:
	s_or_b64 exec, exec, s[2:3]
	s_endpgm
	s_waitcnt vmcnt(0)
	s_barrier
	s_mov_b64 s[0:1], exec
	v_readlane_b32 s2, v242, 7
	v_readlane_b32 s3, v242, 8
	s_and_b64 s[2:3], s[0:1], s[2:3]
	s_mov_b64 exec, s[2:3]
	s_cbranch_execz .LBB0_4113
	s_add_i32 s2, 0, 0x20000
	v_mov_b32_e32 v0, s2
	s_waitcnt vmcnt(0) expcnt(0) lgkmcnt(0)
	ds_read_b32 v2, v0
	s_add_i32 s2, 0, 0x20004
	v_mov_b32_e32 v0, s2
	ds_read_b32 v0, v0
	s_waitcnt lgkmcnt(1)
	v_cmp_ne_u32_e32 vcc, 0, v2
	s_cbranch_vccnz .LBB0_4077
	v_readlane_b32 s2, v242, 9
	v_readlane_b32 s3, v242, 10
	s_load_dwordx2 s[6:7], s[2:3], 0x4
	s_add_u32 s2, s96, 0x1000
	s_addc_u32 s3, s97, 0
	s_add_u32 s4, s96, 0x1100
	s_addc_u32 s5, s97, 0
	v_readlane_b32 s8, v242, 11
	s_waitcnt lgkmcnt(0)
	s_mul_i32 s16, s6, s8
	s_add_u32 s6, s96, 0x1200
	s_mul_i32 s16, s16, s7
	s_addc_u32 s7, s97, 0
	v_readlane_b32 s9, v242, 12
	s_add_u32 s8, s96, 0x1300
	s_addc_u32 s9, s97, 0
	s_mov_b32 s17, 1
	v_mov_b32_e32 v16, 0
	s_branch .LBB0_4065
